# expert-weight conversion stream: next item's 32 loads kept in flight across the current item's transpose and stores (gain load hoisted, per-row waits removed, copies wait vmcnt(4))
# speedup vs baseline: 1.0145x; 1.0145x over previous
; __device__ __forceinline__ void cvt_load(const CvtItem& it, float (&v)[32], int lane) {
; #pragma unroll
;     for (int i = 0; i < 32; ++i) { const int kk = 2 * i + (lane >> 5); v[i] = it.W[(size_t)(it.k0 + kk) * it.N + it.n0 + (lane & 31)]; }
; }
; template <int PH, bool PRB = false>
; __device__ __forceinline__ void run_phase(int layer, LAS unsigned char* lds, const int wv_) {
;     ...
;         if (gi < hi) { CvtItem cur = item_of(gi); float v[32]; cvt_load(cur, v, lane);
.LBB0_1009:
	s_lshl_b64 s[24:25], s[50:51], 2
	v_bfe_u32 v72, v70, 5, 1
	v_and_b32_e32 v0, 31, v70
	s_add_u32 s10, s10, s24
	v_or_b32_e32 v1, s0, v72
	s_addc_u32 s11, s11, s25
	v_lshlrev_b32_e32 v64, 2, v0
	v_lshl_add_u64 v[2:3], s[10:11], 0, v[64:65]
	v_mul_hi_u32_u24_e32 v5, s6, v1
	v_mul_u32_u24_e32 v4, s6, v1
	v_lshl_add_u64 v[4:5], v[4:5], 2, v[2:3]
	global_load_dword v32, v[4:5], off
	v_or_b32_e32 v4, 2, v1
	v_mul_hi_u32_u24_e32 v5, s6, v4
	v_mul_u32_u24_e32 v4, s6, v4
	v_lshl_add_u64 v[4:5], v[4:5], 2, v[2:3]
	global_load_dword v33, v[4:5], off
	v_or_b32_e32 v4, 4, v1
	v_mul_hi_u32_u24_e32 v5, s6, v4
	v_mul_u32_u24_e32 v4, s6, v4
	v_lshl_add_u64 v[4:5], v[4:5], 2, v[2:3]
	global_load_dword v34, v[4:5], off
	v_or_b32_e32 v4, 6, v1
	v_mul_hi_u32_u24_e32 v5, s6, v4
	v_mul_u32_u24_e32 v4, s6, v4
	v_lshl_add_u64 v[4:5], v[4:5], 2, v[2:3]
	global_load_dword v35, v[4:5], off
	v_or_b32_e32 v4, 8, v1
	v_mul_hi_u32_u24_e32 v5, s6, v4
	v_mul_u32_u24_e32 v4, s6, v4
	v_lshl_add_u64 v[4:5], v[4:5], 2, v[2:3]
	global_load_dword v36, v[4:5], off
	v_or_b32_e32 v4, 10, v1
	v_mul_hi_u32_u24_e32 v5, s6, v4
	v_mul_u32_u24_e32 v4, s6, v4
	v_lshl_add_u64 v[4:5], v[4:5], 2, v[2:3]
	global_load_dword v37, v[4:5], off
	v_or_b32_e32 v4, 12, v1
	v_mul_hi_u32_u24_e32 v5, s6, v4
	v_mul_u32_u24_e32 v4, s6, v4
	v_lshl_add_u64 v[4:5], v[4:5], 2, v[2:3]
	global_load_dword v38, v[4:5], off
	v_or_b32_e32 v4, 14, v1
	v_mul_hi_u32_u24_e32 v5, s6, v4
	v_mul_u32_u24_e32 v4, s6, v4
	v_lshl_add_u64 v[4:5], v[4:5], 2, v[2:3]
	global_load_dword v39, v[4:5], off
	v_or_b32_e32 v4, 16, v1
	v_mul_hi_u32_u24_e32 v5, s6, v4
	v_mul_u32_u24_e32 v4, s6, v4
	v_lshl_add_u64 v[4:5], v[4:5], 2, v[2:3]
	global_load_dword v40, v[4:5], off
	v_or_b32_e32 v4, 18, v1
	v_mul_hi_u32_u24_e32 v5, s6, v4
	v_mul_u32_u24_e32 v4, s6, v4
	v_lshl_add_u64 v[4:5], v[4:5], 2, v[2:3]
	global_load_dword v41, v[4:5], off
	v_or_b32_e32 v4, 20, v1
	v_mul_hi_u32_u24_e32 v5, s6, v4
	v_mul_u32_u24_e32 v4, s6, v4
	v_lshl_add_u64 v[4:5], v[4:5], 2, v[2:3]
	global_load_dword v42, v[4:5], off
	v_or_b32_e32 v4, 22, v1
	v_mul_hi_u32_u24_e32 v5, s6, v4
	v_mul_u32_u24_e32 v4, s6, v4
	v_lshl_add_u64 v[4:5], v[4:5], 2, v[2:3]
	global_load_dword v43, v[4:5], off
	v_or_b32_e32 v4, 24, v1
	v_mul_hi_u32_u24_e32 v5, s6, v4
	v_mul_u32_u24_e32 v4, s6, v4
	v_lshl_add_u64 v[4:5], v[4:5], 2, v[2:3]
	global_load_dword v44, v[4:5], off
	v_or_b32_e32 v4, 26, v1
	v_mul_hi_u32_u24_e32 v5, s6, v4
	v_mul_u32_u24_e32 v4, s6, v4
	v_lshl_add_u64 v[4:5], v[4:5], 2, v[2:3]
	global_load_dword v45, v[4:5], off
	v_or_b32_e32 v4, 28, v1
	v_mul_hi_u32_u24_e32 v5, s6, v4
	v_mul_u32_u24_e32 v4, s6, v4
	v_lshl_add_u64 v[4:5], v[4:5], 2, v[2:3]
	global_load_dword v46, v[4:5], off
	v_or_b32_e32 v4, 30, v1
	v_mul_hi_u32_u24_e32 v5, s6, v4
	v_mul_u32_u24_e32 v4, s6, v4
	v_lshl_add_u64 v[4:5], v[4:5], 2, v[2:3]
	global_load_dword v47, v[4:5], off
	v_or_b32_e32 v4, 32, v1
	v_mul_hi_u32_u24_e32 v5, s6, v4
	v_mul_u32_u24_e32 v4, s6, v4
	v_lshl_add_u64 v[4:5], v[4:5], 2, v[2:3]
	global_load_dword v48, v[4:5], off
	v_or_b32_e32 v4, 34, v1
	v_mul_hi_u32_u24_e32 v5, s6, v4
	v_mul_u32_u24_e32 v4, s6, v4
	v_lshl_add_u64 v[4:5], v[4:5], 2, v[2:3]
	global_load_dword v49, v[4:5], off
	v_or_b32_e32 v4, 36, v1
	v_mul_hi_u32_u24_e32 v5, s6, v4
	v_mul_u32_u24_e32 v4, s6, v4
	v_lshl_add_u64 v[4:5], v[4:5], 2, v[2:3]
	global_load_dword v50, v[4:5], off
	v_or_b32_e32 v4, 38, v1
	v_mul_hi_u32_u24_e32 v5, s6, v4
	v_mul_u32_u24_e32 v4, s6, v4
	v_lshl_add_u64 v[4:5], v[4:5], 2, v[2:3]
	global_load_dword v51, v[4:5], off
	v_or_b32_e32 v4, 40, v1
	v_mul_hi_u32_u24_e32 v5, s6, v4
	v_mul_u32_u24_e32 v4, s6, v4
	v_lshl_add_u64 v[4:5], v[4:5], 2, v[2:3]
	global_load_dword v52, v[4:5], off
	v_or_b32_e32 v4, 42, v1
	v_mul_hi_u32_u24_e32 v5, s6, v4
	v_mul_u32_u24_e32 v4, s6, v4
	v_lshl_add_u64 v[4:5], v[4:5], 2, v[2:3]
	global_load_dword v53, v[4:5], off
	v_or_b32_e32 v4, 44, v1
	v_mul_hi_u32_u24_e32 v5, s6, v4
	v_mul_u32_u24_e32 v4, s6, v4
	v_lshl_add_u64 v[4:5], v[4:5], 2, v[2:3]
	global_load_dword v54, v[4:5], off
	v_or_b32_e32 v4, 46, v1
	v_mul_hi_u32_u24_e32 v5, s6, v4
	v_mul_u32_u24_e32 v4, s6, v4
	v_lshl_add_u64 v[4:5], v[4:5], 2, v[2:3]
	global_load_dword v55, v[4:5], off
	v_or_b32_e32 v4, 48, v1
	v_mul_hi_u32_u24_e32 v5, s6, v4
	v_mul_u32_u24_e32 v4, s6, v4
	v_lshl_add_u64 v[4:5], v[4:5], 2, v[2:3]
	global_load_dword v56, v[4:5], off
	v_or_b32_e32 v4, 50, v1
	v_mul_hi_u32_u24_e32 v5, s6, v4
	v_mul_u32_u24_e32 v4, s6, v4
	v_lshl_add_u64 v[4:5], v[4:5], 2, v[2:3]
	global_load_dword v57, v[4:5], off
	v_or_b32_e32 v4, 52, v1
	v_mul_hi_u32_u24_e32 v5, s6, v4
	v_mul_u32_u24_e32 v4, s6, v4
	v_lshl_add_u64 v[4:5], v[4:5], 2, v[2:3]
	global_load_dword v58, v[4:5], off
	v_or_b32_e32 v4, 54, v1
	v_mul_hi_u32_u24_e32 v5, s6, v4
	v_mul_u32_u24_e32 v4, s6, v4
	v_lshl_add_u64 v[4:5], v[4:5], 2, v[2:3]
	global_load_dword v59, v[4:5], off
	v_or_b32_e32 v4, 56, v1
	v_mul_hi_u32_u24_e32 v5, s6, v4
	v_mul_u32_u24_e32 v4, s6, v4
	v_lshl_add_u64 v[4:5], v[4:5], 2, v[2:3]
	global_load_dword v60, v[4:5], off
	v_or_b32_e32 v4, 58, v1
	v_mul_hi_u32_u24_e32 v5, s6, v4
	v_mul_u32_u24_e32 v4, s6, v4
	v_lshl_add_u64 v[4:5], v[4:5], 2, v[2:3]
	global_load_dword v61, v[4:5], off
	v_or_b32_e32 v4, 60, v1
	v_mul_hi_u32_u24_e32 v5, s6, v4
	v_mul_u32_u24_e32 v4, s6, v4
	v_lshl_add_u64 v[4:5], v[4:5], 2, v[2:3]
	v_or_b32_e32 v1, 62, v1
	global_load_dword v62, v[4:5], off
	v_mul_hi_u32_u24_e32 v5, s6, v1
	v_mul_u32_u24_e32 v4, s6, v1
	v_lshl_add_u64 v[2:3], v[4:5], 2, v[2:3]
	global_load_dword v63, v[2:3], off
	s_add_u32 s37, s4, s20
	v_lshlrev_b32_e32 v3, 3, v70
	v_readlane_b32 s6, v254, 9
	s_addc_u32 s38, s5, s21
	v_bfe_u32 v73, v70, 3, 3
	v_and_b32_e32 v66, 56, v3
	v_and_b32_e32 v71, 63, v70
	v_add_u32_e32 v1, s6, v64
	v_mul_u32_u24_e32 v2, 0x84, v72
	s_add_u32 s39, s16, 0x20400000
	v_mul_u32_u24_e32 v3, 0x84, v66
	v_lshlrev_b32_e32 v4, 2, v73
	s_addc_u32 s40, s17, 0
	v_cmp_gt_u32_e64 s[4:5], 32, v71
	v_add3_u32 v74, s6, v3, v4
	v_mov_b32_e32 v67, v65
	v_or_b32_e32 v75, 8, v73
	v_or_b32_e32 v76, 16, v73
	v_or_b32_e32 v77, 24, v73
	v_lshlrev_b32_e32 v64, 2, v0
	v_add_u32_e32 v78, v1, v2
	s_mov_b32 s46, s50
	s_waitcnt vmcnt(0)
	s_branch .LBB0_1011

; __device__ __forceinline__ void cvt_finish(const CvtItem& it, float (&v)[32], LAS float* scr, int lane) {
;     if (it.g) { const float gv = it.g[it.k0 + lane];
; template <int PH, bool PRB = false>
; __device__ __forceinline__ void run_phase(int layer, LAS unsigned char* lds, const int wv_) {
;     ...
;             for (;;) { const int gn = gi + CNGW; const bool more = gn < hi; CvtItem nxt = item_of(more ? gn : gi); float vn[32];
;                 if (more) cvt_load(nxt, vn, lane);
.LBB0_1011:
	s_cmp_eq_u64 s[8:9], 0
	s_cbranch_scc1 .Lcv_nog
	v_add_u32_e32 v84, s0, v71
	v_mov_b32_e32 v85, v65
	v_lshl_add_u64 v[84:85], v[84:85], 2, s[8:9]
	global_load_dword v82, v[84:85], off

; __device__ __forceinline__ void cvt_finish(const CvtItem& it, float (&v)[32], LAS float* scr, int lane) {
;     if (it.g) { const float gv = it.g[it.k0 + lane];
; #pragma unroll
;         for (int i = 0; i < 32; ++i) { const float g0 = __builtin_bit_cast(float, __builtin_amdgcn_readlane(__builtin_bit_cast(int, gv), 2 * i)), g1 = __builtin_bit_cast(float, __builtin_amdgcn_readlane(__builtin_bit_cast(int, gv), 2 * i + 1)); v[i] *= (lane >> 5) ? g1 : g0; } }
.LBB0_1017:
	s_cmp_eq_u64 s[8:9], 0
	s_cbranch_scc1 .LBB0_1019
	s_and_b64 vcc, exec, s[6:7]
	s_cbranch_vccz .Lcv_w32
	s_waitcnt vmcnt(0)
	s_branch .Lcv_wd
.Lcv_w32:
	s_waitcnt vmcnt(32)
.Lcv_wd:
	v_mov_b32_e32 v68, v82
	s_nop 0
	v_readlane_b32 s8, v68, 0
	v_readlane_b32 s9, v68, 1
	s_nop 0
	v_mov_b32_e32 v79, s8
	v_readlane_b32 s8, v68, 2
	v_mov_b32_e32 v69, s9
	v_cndmask_b32_e64 v69, v69, v79, s[4:5]
	v_readlane_b32 s9, v68, 3
	v_mul_f32_e32 v32, v32, v69
	v_mov_b32_e32 v79, s8
	v_mov_b32_e32 v69, s9
	v_cndmask_b32_e64 v69, v69, v79, s[4:5]
	v_readlane_b32 s8, v68, 4
	v_readlane_b32 s9, v68, 5
	v_mul_f32_e32 v33, v33, v69
	v_mov_b32_e32 v79, s8
	v_mov_b32_e32 v69, s9
	v_cndmask_b32_e64 v69, v69, v79, s[4:5]
	v_readlane_b32 s8, v68, 6
	v_readlane_b32 s9, v68, 7
	s_waitcnt lgkmcnt(0)
	v_mul_f32_e32 v34, v34, v69
	v_mov_b32_e32 v79, s8
	v_mov_b32_e32 v69, s9
	v_cndmask_b32_e64 v69, v69, v79, s[4:5]
	v_readlane_b32 s8, v68, 8
	v_readlane_b32 s9, v68, 9
	v_mul_f32_e32 v35, v35, v69
	v_mov_b32_e32 v79, s8
	v_mov_b32_e32 v69, s9
	v_cndmask_b32_e64 v69, v69, v79, s[4:5]
	v_readlane_b32 s8, v68, 10
	v_readlane_b32 s9, v68, 11
	v_mul_f32_e32 v36, v36, v69
	v_mov_b32_e32 v79, s8
	v_mov_b32_e32 v69, s9
	v_cndmask_b32_e64 v69, v69, v79, s[4:5]
	v_readlane_b32 s8, v68, 12
	v_readlane_b32 s9, v68, 13
	v_mul_f32_e32 v37, v37, v69
	v_mov_b32_e32 v79, s8
	v_mov_b32_e32 v69, s9
	v_cndmask_b32_e64 v69, v69, v79, s[4:5]
	v_readlane_b32 s8, v68, 14
	v_readlane_b32 s9, v68, 15
	v_mul_f32_e32 v38, v38, v69
	v_mov_b32_e32 v79, s8
	v_mov_b32_e32 v69, s9
	v_cndmask_b32_e64 v69, v69, v79, s[4:5]
	v_readlane_b32 s8, v68, 16
	v_readlane_b32 s9, v68, 17
	v_mul_f32_e32 v39, v39, v69
	v_mov_b32_e32 v79, s8
	v_mov_b32_e32 v69, s9
	v_cndmask_b32_e64 v69, v69, v79, s[4:5]
	v_readlane_b32 s8, v68, 18
	v_readlane_b32 s9, v68, 19
	v_mul_f32_e32 v40, v40, v69
	v_mov_b32_e32 v79, s8
	v_mov_b32_e32 v69, s9
	v_cndmask_b32_e64 v69, v69, v79, s[4:5]
	v_readlane_b32 s8, v68, 20
	v_readlane_b32 s9, v68, 21
	v_mul_f32_e32 v41, v41, v69
	v_mov_b32_e32 v79, s8
	v_mov_b32_e32 v69, s9
	v_cndmask_b32_e64 v69, v69, v79, s[4:5]
	v_readlane_b32 s8, v68, 22
	v_readlane_b32 s9, v68, 23
	v_mul_f32_e32 v42, v42, v69
	v_mov_b32_e32 v79, s8
	v_mov_b32_e32 v69, s9
	v_cndmask_b32_e64 v69, v69, v79, s[4:5]
	v_readlane_b32 s8, v68, 24
	v_readlane_b32 s9, v68, 25
	v_mul_f32_e32 v43, v43, v69
	v_mov_b32_e32 v79, s8
	v_mov_b32_e32 v69, s9
	v_cndmask_b32_e64 v69, v69, v79, s[4:5]
	v_readlane_b32 s8, v68, 26
	v_readlane_b32 s9, v68, 27
	v_mul_f32_e32 v44, v44, v69
	v_mov_b32_e32 v79, s8
	v_mov_b32_e32 v69, s9
	v_cndmask_b32_e64 v69, v69, v79, s[4:5]
	v_readlane_b32 s8, v68, 28
	v_readlane_b32 s9, v68, 29
	v_mul_f32_e32 v45, v45, v69
	v_mov_b32_e32 v79, s8
	v_mov_b32_e32 v69, s9
	v_cndmask_b32_e64 v69, v69, v79, s[4:5]
	v_readlane_b32 s8, v68, 30
	v_readlane_b32 s9, v68, 31
	v_mul_f32_e32 v46, v46, v69
	v_mov_b32_e32 v79, s8
	v_mov_b32_e32 v69, s9
	v_cndmask_b32_e64 v69, v69, v79, s[4:5]
	v_readlane_b32 s8, v68, 32
	v_readlane_b32 s9, v68, 33
	v_mul_f32_e32 v47, v47, v69
	v_mov_b32_e32 v79, s8
	v_mov_b32_e32 v69, s9
	v_cndmask_b32_e64 v69, v69, v79, s[4:5]
	v_readlane_b32 s8, v68, 34
	v_readlane_b32 s9, v68, 35
	v_mul_f32_e32 v48, v48, v69
	v_mov_b32_e32 v79, s8
	v_mov_b32_e32 v69, s9
	v_cndmask_b32_e64 v69, v69, v79, s[4:5]
	v_readlane_b32 s8, v68, 36
	v_readlane_b32 s9, v68, 37
	v_mul_f32_e32 v49, v49, v69
	v_mov_b32_e32 v79, s8
	v_mov_b32_e32 v69, s9
	v_cndmask_b32_e64 v69, v69, v79, s[4:5]
	v_readlane_b32 s8, v68, 38
	v_readlane_b32 s9, v68, 39
	v_mul_f32_e32 v50, v50, v69
	v_mov_b32_e32 v79, s8
	v_mov_b32_e32 v69, s9
	v_cndmask_b32_e64 v69, v69, v79, s[4:5]
	v_readlane_b32 s8, v68, 40
	v_readlane_b32 s9, v68, 41
	v_mul_f32_e32 v51, v51, v69
	v_mov_b32_e32 v79, s8
	v_mov_b32_e32 v69, s9
	v_cndmask_b32_e64 v69, v69, v79, s[4:5]
	v_readlane_b32 s8, v68, 42
	v_readlane_b32 s9, v68, 43
	v_mul_f32_e32 v52, v52, v69
	v_mov_b32_e32 v79, s8
	v_mov_b32_e32 v69, s9
	v_cndmask_b32_e64 v69, v69, v79, s[4:5]
	v_readlane_b32 s8, v68, 44
	v_readlane_b32 s9, v68, 45
	v_mul_f32_e32 v53, v53, v69
	v_mov_b32_e32 v79, s8
	v_mov_b32_e32 v69, s9
	v_cndmask_b32_e64 v69, v69, v79, s[4:5]
	v_readlane_b32 s8, v68, 46
	v_readlane_b32 s9, v68, 47
	v_mul_f32_e32 v54, v54, v69
	v_mov_b32_e32 v79, s8
	v_mov_b32_e32 v69, s9
	v_cndmask_b32_e64 v69, v69, v79, s[4:5]
	v_readlane_b32 s8, v68, 48
	v_readlane_b32 s9, v68, 49
	v_mul_f32_e32 v55, v55, v69
	v_mov_b32_e32 v79, s8
	v_mov_b32_e32 v69, s9
	v_cndmask_b32_e64 v69, v69, v79, s[4:5]
	v_readlane_b32 s8, v68, 50
	v_readlane_b32 s9, v68, 51
	v_mul_f32_e32 v56, v56, v69
	v_mov_b32_e32 v79, s8
	v_mov_b32_e32 v69, s9
	v_cndmask_b32_e64 v69, v69, v79, s[4:5]
	v_readlane_b32 s8, v68, 52
	v_readlane_b32 s9, v68, 53
	v_mul_f32_e32 v57, v57, v69
	v_mov_b32_e32 v79, s8
	v_mov_b32_e32 v69, s9
	v_cndmask_b32_e64 v69, v69, v79, s[4:5]
	v_readlane_b32 s8, v68, 54
	v_readlane_b32 s9, v68, 55
	v_mul_f32_e32 v58, v58, v69
	v_mov_b32_e32 v79, s8
	v_mov_b32_e32 v69, s9
	v_cndmask_b32_e64 v69, v69, v79, s[4:5]
	v_readlane_b32 s8, v68, 56
	v_readlane_b32 s9, v68, 57
	v_mul_f32_e32 v59, v59, v69
	v_mov_b32_e32 v79, s8
	v_mov_b32_e32 v69, s9
	v_cndmask_b32_e64 v69, v69, v79, s[4:5]
	v_readlane_b32 s8, v68, 58
	v_readlane_b32 s9, v68, 59
	v_mul_f32_e32 v60, v60, v69
	v_mov_b32_e32 v79, s8
	v_mov_b32_e32 v69, s9
	v_cndmask_b32_e64 v69, v69, v79, s[4:5]
	v_readlane_b32 s8, v68, 60
	v_readlane_b32 s9, v68, 61
	v_mul_f32_e32 v61, v61, v69
	v_mov_b32_e32 v79, s8
	v_mov_b32_e32 v69, s9
	v_cndmask_b32_e64 v69, v69, v79, s[4:5]
	v_readlane_b32 s8, v68, 62
	v_readlane_b32 s9, v68, 63
	v_mul_f32_e32 v62, v62, v69
	v_mov_b32_e32 v69, s8
	v_mov_b32_e32 v68, s9
	v_cndmask_b32_e64 v68, v68, v69, s[4:5]
	v_mul_f32_e32 v63, v63, v68
; #define LAS __attribute__((address_space(3)))
; #define CVT_PK_FP8_SAT(a, b, old, hi) __builtin_amdgcn_cvt_pk_fp8_f32(__builtin_amdgcn_fmed3f((a), -448.0f, 448.0f), __builtin_amdgcn_fmed3f((b), -448.0f, 448.0f), (old), (hi))
; __device__ __forceinline__ void cvt_finish(const CvtItem& it, float (&v)[32], LAS float* scr, int lane) {
;     ...
; #pragma unroll
;     for (int i = 0; i < 32; ++i) { const int kk = 2 * i + (lane >> 5); scr[kk * 33 + (lane & 31)] = v[i]; }
;     asm volatile("s_waitcnt lgkmcnt(0)" ::: "memory");
;     const int c = lane & 7;
; #pragma unroll
;     for (int j = 0; j < 4; ++j) { const int n = it.n0 + (lane >> 3) + 8 * j; const LAS float* s = scr + (8 * c) * 33 + (lane >> 3) + 8 * j;
;         const int row = it.rowmode == 0 ? n : ((n >> 7) * 256 + (it.rowmode == 2 ? 128 : 0) + (n & 127));
;         if (it.fp8) { int w0 = CVT_PK_FP8_SAT(s[0 * 33] * FP8_WSCALE, s[1 * 33] * FP8_WSCALE, 0, false); w0 = CVT_PK_FP8_SAT(s[2 * 33] * FP8_WSCALE, s[3 * 33] * FP8_WSCALE, w0, true);
;             int w1 = CVT_PK_FP8_SAT(s[4 * 33] * FP8_WSCALE, s[5 * 33] * FP8_WSCALE, 0, false); w1 = CVT_PK_FP8_SAT(s[6 * 33] * FP8_WSCALE, s[7 * 33] * FP8_WSCALE, w1, true);
;             u32x2 o8; o8.x = (unsigned)w0; o8.y = (unsigned)w1; *(u32x2*)((unsigned char*)it.WT + (size_t)row * it.K + it.k0 + 8 * c) = o8; continue; }
.LBB0_1019:
	ds_write2_b32 v78, v32, v33 offset1:66
	s_waitcnt lgkmcnt(0)
	ds_write2_b32 v78, v34, v35 offset0:132 offset1:198
	v_add_u32_e32 v32, 0x400, v78
	ds_write2_b32 v32, v36, v37 offset0:8 offset1:74
	ds_write2_b32 v32, v38, v39 offset0:140 offset1:206
	v_add_u32_e32 v32, 0x800, v78
	ds_write2_b32 v32, v40, v41 offset0:16 offset1:82
	ds_write2_b32 v32, v42, v43 offset0:148 offset1:214
	v_add_u32_e32 v32, 0xc00, v78
	ds_write2_b32 v32, v44, v45 offset0:24 offset1:90
	ds_write2_b32 v32, v46, v47 offset0:156 offset1:222
	v_add_u32_e32 v32, 0x1000, v78
	ds_write2_b32 v32, v48, v49 offset0:32 offset1:98
	ds_write2_b32 v32, v50, v51 offset0:164 offset1:230
	v_add_u32_e32 v32, 0x1400, v78
	ds_write2_b32 v32, v52, v53 offset0:40 offset1:106
	ds_write2_b32 v32, v54, v55 offset0:172 offset1:238
	v_add_u32_e32 v32, 0x1800, v78
	ds_write2_b32 v32, v56, v57 offset0:48 offset1:114
	ds_write2_b32 v32, v58, v59 offset0:180 offset1:246
	v_add_u32_e32 v32, 0x1c00, v78
	ds_write2_b32 v32, v60, v61 offset0:56 offset1:122
	ds_write2_b32 v32, v62, v63 offset0:188 offset1:254
	v_add_u32_e32 v32, s46, v73
	s_cmp_eq_u32 s47, 0
	s_cselect_b64 s[8:9], -1, 0
	v_lshlrev_b32_e32 v33, 1, v32
	s_cmp_eq_u32 s47, 2
	s_waitcnt lgkmcnt(0)
	v_and_b32_e32 v33, 0x7fffff00, v33
	s_cselect_b32 s30, 0x80, 0
	v_and_b32_e32 v34, 0x7f, v32
	v_or3_b32 v33, v33, v34, s30
	ds_read_b32 v34, v74
	s_cmp_lg_u32 s1, 0
	s_cselect_b64 s[28:29], -1, 0
	s_cmp_eq_u32 s1, 0
	v_cndmask_b32_e64 v33, v33, v32, s[8:9]
	s_cbranch_scc1 .LBB0_1033
	ds_read2_b32 v[36:37], v74 offset0:33 offset1:66
	ds_read2_b32 v[38:39], v74 offset0:99 offset1:132
	s_waitcnt lgkmcnt(0)
	v_mul_f32_e32 v32, 0x42800000, v34
	v_med3_f32 v32, v32, s97, v219
	s_mov_b32 s1, s51
	v_mul_f32_e32 v35, 0x42800000, v36
	v_med3_f32 v35, v35, s97, v219
	v_mov_b32_e32 v36, v65
	v_cvt_pk_fp8_f32 v36, v32, v35
	v_mul_f32_e32 v32, 0x42800000, v37
	v_mul_f32_e32 v35, 0x42800000, v38
	v_med3_f32 v32, v32, s97, v219
	v_med3_f32 v35, v35, s97, v219
	v_cvt_pk_fp8_f32 v36, v32, v35 op_sel:[0,0,1]
	v_mul_f32_e32 v32, 0x42800000, v39
	ds_read2_b32 v[38:39], v74 offset0:165 offset1:198
	v_med3_f32 v32, v32, s97, v219
	v_mov_b32_e32 v37, v65
	s_waitcnt lgkmcnt(0)
	v_mul_f32_e32 v35, 0x42800000, v38
	v_med3_f32 v35, v35, s97, v219
	v_cvt_pk_fp8_f32 v37, v32, v35
	ds_read_b32 v35, v74 offset:924
	v_mul_f32_e32 v32, 0x42800000, v39
	v_med3_f32 v32, v32, s97, v219
	v_mov_b64_e32 v[38:39], s[22:23]
	v_mad_u64_u32 v[38:39], s[10:11], v33, s19, v[38:39]
	s_waitcnt lgkmcnt(0)
	v_mul_f32_e32 v35, 0x42800000, v35
	v_med3_f32 v35, v35, s97, v219
	v_cvt_pk_fp8_f32 v37, v32, v35 op_sel:[0,0,1]
	v_lshl_add_u64 v[38:39], v[38:39], 0, s[0:1]
	v_lshl_add_u64 v[38:39], v[38:39], 0, v[66:67]
	global_store_dwordx2 v[38:39], v[36:37], off
	v_lshlrev_b32_e32 v32, 1, v66
	s_cbranch_execnz .LBB0_1022

; template <int PH, bool PRB = false>
; __device__ __forceinline__ void run_phase(int layer, LAS unsigned char* lds, const int wv_) {
;     ...
;                 cvt_finish(cur, v, scr, lane);
;                 if (!more) break;
; #pragma unroll
;                 for (int i = 0; i < 32; ++i) v[i] = vn[i];
;                 cur = nxt; gi = gn; } }
.LBB0_1031:
	s_waitcnt lgkmcnt(0)
	s_and_b64 vcc, exec, s[6:7]
	s_mov_b64 s[0:1], -1
	s_cbranch_vccnz .LBB0_1010
	v_readlane_b32 s0, v254, 17
	s_waitcnt vmcnt(4)
	s_waitcnt lgkmcnt(0)
	v_mov_b64_e32 v[62:63], v[30:31]
	s_add_i32 s33, s33, s0
	s_mov_b64 s[0:1], 0
	v_mov_b64_e32 v[60:61], v[28:29]
	v_mov_b64_e32 v[58:59], v[26:27]
	v_mov_b64_e32 v[56:57], v[24:25]
	v_mov_b64_e32 v[54:55], v[22:23]
	v_mov_b64_e32 v[52:53], v[20:21]
	v_mov_b64_e32 v[50:51], v[18:19]
	v_mov_b64_e32 v[48:49], v[16:17]
	v_mov_b64_e32 v[46:47], v[14:15]
	v_mov_b64_e32 v[44:45], v[12:13]
	v_mov_b64_e32 v[42:43], v[10:11]
	v_mov_b64_e32 v[40:41], v[8:9]
	v_mov_b64_e32 v[38:39], v[6:7]
	v_mov_b64_e32 v[36:37], v[4:5]
	v_mov_b64_e32 v[34:35], v[2:3]
	v_mov_b64_e32 v[32:33], v[0:1]
	s_branch .LBB0_1010
